# GDN loop: next-item register prefetch moved from the head of section c to section d for waves 1-7 (idle there); wave 0 keeps it in c
# speedup vs baseline: 1.0071x; 1.0071x over previous
.LBB0_233:
	v_lshlrev_b32_e32 v68, 16, v39
	v_and_b32_e32 v69, 0xffff0000, v39
	v_lshlrev_b32_e32 v74, 16, v42
	v_and_b32_e32 v75, 0xffff0000, v42
	v_xor_b32_e32 v39, 32, v209
	v_add_u32_e32 v42, 64, v100
	v_cmp_lt_i32_e32 vcc, v39, v42
	v_lshlrev_b32_e32 v108, 16, v28
	v_and_b32_e32 v109, 0xffff0000, v28
	v_cndmask_b32_e32 v39, v209, v39, vcc
	v_lshlrev_b32_e32 v105, 2, v39
	v_xor_b32_e32 v39, 16, v209
	v_cmp_lt_i32_e32 vcc, v39, v42
	v_lshlrev_b32_e32 v85, 16, v41
	v_and_b32_e32 v81, 0xffff0000, v41
	v_cndmask_b32_e32 v39, v209, v39, vcc
	v_lshlrev_b32_e32 v103, 2, v39
	v_xor_b32_e32 v39, 8, v209
	v_cmp_lt_i32_e32 vcc, v39, v42
	v_lshlrev_b32_e32 v78, 16, v40
	v_and_b32_e32 v79, 0xffff0000, v40
	v_cndmask_b32_e32 v39, v209, v39, vcc
	v_lshlrev_b32_e32 v102, 2, v39
	v_xor_b32_e32 v39, 4, v209
	v_cmp_lt_i32_e32 vcc, v39, v42
	v_lshlrev_b32_e32 v40, 16, v97
	v_and_b32_e32 v41, 0xffff0000, v97
	v_cndmask_b32_e32 v39, v209, v39, vcc
	v_lshlrev_b32_e32 v101, 2, v39
	v_xor_b32_e32 v39, 2, v209
	v_cmp_lt_i32_e32 vcc, v39, v42
	v_lshl_add_u32 v97, v38, 1, 0
	v_bitop3_b32 v38, v215, s82, 7 bitop3:0x6c
	v_cndmask_b32_e32 v39, v209, v39, vcc
	v_lshlrev_b32_e32 v100, 2, v39
	v_xor_b32_e32 v39, 1, v209
	v_cmp_lt_i32_e32 vcc, v39, v42
	v_lshlrev_b32_e32 v116, 16, v32
	v_and_b32_e32 v117, 0xffff0000, v32
	v_cndmask_b32_e32 v39, v209, v39, vcc
	v_lshlrev_b32_e32 v84, 16, v36
	v_and_b32_e32 v91, 0xffff0000, v36
	v_lshlrev_b32_e32 v58, 16, v35
	v_and_b32_e32 v59, 0xffff0000, v35
	v_lshlrev_b32_e32 v66, 16, v37
	v_and_b32_e32 v67, 0xffff0000, v37
	v_lshlrev_b32_e32 v76, 16, v46
	v_and_b32_e32 v77, 0xffff0000, v46
	v_lshlrev_b32_e32 v54, 16, v47
	v_and_b32_e32 v55, 0xffff0000, v47
	v_lshlrev_b32_e32 v46, 16, v52
	v_and_b32_e32 v47, 0xffff0000, v52
	v_lshlrev_b32_e32 v34, 16, v53
	v_and_b32_e32 v35, 0xffff0000, v53
	v_lshlrev_b32_e32 v36, 16, v92
	v_and_b32_e32 v37, 0xffff0000, v92
	v_lshlrev_b32_e32 v52, 16, v98
	v_and_b32_e32 v53, 0xffff0000, v98
	v_lshlrev_b32_e32 v98, 2, v39
	v_lshlrev_b32_e32 v92, 3, v38
	v_pk_fma_f32 v[38:39], v[16:17], v[108:109], 0 op_sel_hi:[1,1,0]
	v_lshlrev_b32_e32 v62, 16, v30
	v_and_b32_e32 v63, 0xffff0000, v30
	v_pk_fma_f32 v[38:39], v[18:19], v[116:117], v[38:39]
	v_lshlrev_b32_e32 v106, 16, v27
	v_pk_fma_f32 v[38:39], v[20:21], v[62:63], v[38:39]
	v_and_b32_e32 v107, 0xffff0000, v27
	v_pk_fma_f32 v[38:39], v[22:23], v[68:69], v[38:39]
	v_lshlrev_b32_e32 v87, 16, v43
	v_and_b32_e32 v83, 0xffff0000, v43
	v_mul_f32_e32 v42, 0xbfb8aa3b, v38
	v_mul_f32_e32 v43, 0xbfb8aa3b, v39
	v_lshlrev_b32_e32 v114, 16, v31
	v_and_b32_e32 v115, 0xffff0000, v31
	v_lshlrev_b32_e32 v72, 16, v44
	v_and_b32_e32 v73, 0xffff0000, v44
	v_lshlrev_b32_e32 v70, 16, v45
	v_and_b32_e32 v64, 0xffff0000, v45
	v_exp_f32_e32 v42, v42
	v_exp_f32_e32 v43, v43
	v_pk_fma_f32 v[44:45], v[8:9], v[106:107], 0 op_sel_hi:[1,1,0]
	v_lshlrev_b32_e32 v112, 16, v29
	v_pk_fma_f32 v[44:45], v[10:11], v[114:115], v[44:45]
	v_and_b32_e32 v88, 0xffff0000, v29
	v_pk_fma_f32 v[44:45], v[12:13], v[58:59], v[44:45]
	v_lshlrev_b32_e32 v71, 16, v49
	v_pk_fma_f32 v[44:45], v[14:15], v[66:67], v[44:45]
	v_and_b32_e32 v65, 0xffff0000, v49
	v_lshlrev_b32_e32 v60, 16, v48
	v_and_b32_e32 v61, 0xffff0000, v48
	v_lshlrev_b32_e32 v29, 16, v57
	v_and_b32_e32 v25, 0xffff0000, v57
	v_lshlrev_b32_e32 v48, 16, v56
	v_and_b32_e32 v49, 0xffff0000, v56
	v_add_f32_e32 v42, 1.0, v42
	v_add_f32_e32 v43, 1.0, v43
	v_mul_f32_e32 v56, 0xbfb8aa3b, v44
	v_mul_f32_e32 v57, 0xbfb8aa3b, v45
	v_rcp_f32_e32 v42, v42
	v_rcp_f32_e32 v43, v43
	v_exp_f32_e32 v56, v56
	v_exp_f32_e32 v57, v57
	v_lshlrev_b32_e32 v113, 16, v33
	v_pk_mul_f32 v[38:39], v[38:39], v[42:43]
	v_add_f32_e32 v42, 1.0, v56
	v_add_f32_e32 v43, 1.0, v57
	v_rcp_f32_e32 v42, v42
	v_rcp_f32_e32 v43, v43
	v_pk_mul_f32 v[56:57], v[38:39], v[38:39]
	v_mov_b32_e32 v86, v85
	v_add_f32_e32 v119, v56, v57
	v_pk_mul_f32 v[44:45], v[44:45], v[42:43]
	v_pk_fma_f32 v[42:43], v[16:17], v[116:117], 0 op_sel_hi:[1,1,0]
	s_waitcnt lgkmcnt(0)
	v_mul_f32_e32 v24, 0xbfb8aa3b, v26
	v_pk_fma_f32 v[42:43], v[18:19], v[62:63], v[42:43]
	v_exp_f32_e32 v24, v24
	v_pk_fma_f32 v[42:43], v[20:21], v[68:69], v[42:43]
	v_and_b32_e32 v89, 0xffff0000, v33
	v_pk_fma_f32 v[42:43], v[22:23], v[74:75], v[42:43]
	v_add_f32_e32 v24, 1.0, v24
	v_mul_f32_e32 v56, 0xbfb8aa3b, v42
	v_exp_f32_e32 v106, v56
	v_mul_f32_e32 v56, 0xbfb8aa3b, v43
	v_exp_f32_e32 v107, v56
	v_pk_mul_f32 v[56:57], v[44:45], v[44:45]
	v_add_f32_e32 v106, 1.0, v106
	v_rcp_f32_e32 v106, v106
	v_add_f32_e32 v107, 1.0, v107
	v_rcp_f32_e32 v107, v107
	v_add_f32_e32 v116, v56, v57
	v_rcp_f32_e32 v95, v24
	v_mov_b32_e32 v90, v89
	v_pk_mul_f32 v[42:43], v[42:43], v[106:107]
	v_pk_fma_f32 v[88:89], v[0:1], v[88:89], 0 op_sel:[1,0,0] op_sel_hi:[1,1,0]
	v_pk_mul_f32 v[56:57], v[42:43], v[42:43]
	v_mov_b32_e32 v80, v91
	v_add_f32_e32 v117, v56, v57
	v_pk_fma_f32 v[56:57], v[8:9], v[114:115], 0 op_sel_hi:[1,1,0]
	v_mov_b32_e32 v114, v113
	v_pk_fma_f32 v[56:57], v[10:11], v[58:59], v[56:57]
	v_mov_b32_e32 v115, v84
	v_pk_fma_f32 v[56:57], v[12:13], v[66:67], v[56:57]
	v_pk_fma_f32 v[112:113], v[0:1], v[112:113], 0 op_sel_hi:[0,1,0]
	v_pk_fma_f32 v[56:57], v[14:15], v[78:79], v[56:57]
	v_pk_fma_f32 v[112:113], v[2:3], v[114:115], v[112:113] op_sel_hi:[0,1,1]
	v_mul_f32_e32 v106, 0xbfb8aa3b, v56
	v_exp_f32_e32 v107, v106
	v_mul_f32_e32 v106, 0xbfb8aa3b, v57
	v_exp_f32_e32 v109, v106
	v_pk_fma_f32 v[112:113], v[4:5], v[84:85], v[112:113] op_sel_hi:[0,1,1]
	v_add_f32_e32 v107, 1.0, v107
	v_pk_fma_f32 v[112:113], v[6:7], v[86:87], v[112:113] op_sel_hi:[0,1,1]
	v_rcp_f32_e32 v108, v107
	v_add_f32_e32 v107, 1.0, v109
	v_mul_f32_e32 v109, 0xbfb8aa3b, v112
	v_exp_f32_e32 v110, v109
	v_mul_f32_e32 v109, 0xbfb8aa3b, v113
	v_exp_f32_e32 v115, v109
	v_rcp_f32_e32 v109, v107
	v_add_f32_e32 v107, 1.0, v110
	v_rcp_f32_e32 v114, v107
	v_add_f32_e32 v107, 1.0, v115
	v_rcp_f32_e32 v115, v107
	v_pk_mul_f32 v[56:57], v[56:57], v[108:109]
	v_readlane_b32 s2, v95, s95
	v_pk_mul_f32 v[108:109], v[56:57], v[56:57]
	v_readlane_b32 s3, v95, s54
	v_add_f32_e32 v120, v108, v109
	v_pk_mul_f32 v[108:109], v[112:113], v[114:115]
	v_pk_fma_f32 v[88:89], v[2:3], v[90:91], v[88:89] op_sel:[1,0,0]
	v_mov_b32_e32 v82, v81
	v_pk_mul_f32 v[108:109], v[108:109], s[2:3]
	v_pk_fma_f32 v[88:89], v[4:5], v[80:81], v[88:89] op_sel:[1,0,0]
	v_cvt_pk_bf16_f32 v107, v108, v109
	v_pk_fma_f32 v[108:109], v[6:7], v[82:83], v[88:89] op_sel:[1,0,0]
	v_pk_fma_f32 v[62:63], v[16:17], v[62:63], 0 op_sel_hi:[1,1,0]
	v_mul_f32_e32 v88, 0xbfb8aa3b, v108
	v_exp_f32_e32 v88, v88
	v_mul_f32_e32 v89, 0xbfb8aa3b, v109
	v_exp_f32_e32 v89, v89
	v_pk_fma_f32 v[62:63], v[18:19], v[68:69], v[62:63]
	v_lshlrev_b32_e32 v32, 16, v50
	v_and_b32_e32 v33, 0xffff0000, v50
	v_lshlrev_b32_e32 v28, 16, v51
	v_and_b32_e32 v24, 0xffff0000, v51
	v_lshlrev_b32_e32 v50, 16, v93
	v_and_b32_e32 v51, 0xffff0000, v93
	v_mul_lo_u32 v93, v215, s11
	v_add_f32_e32 v88, 1.0, v88
	v_pk_fma_f32 v[62:63], v[20:21], v[74:75], v[62:63]
	v_add_lshl_u32 v90, v92, v93, 1
	v_rcp_f32_e32 v112, v88
	v_add_f32_e32 v88, 1.0, v89
	v_pk_fma_f32 v[62:63], v[22:23], v[76:77], v[62:63]
	v_rcp_f32_e32 v113, v88
	v_add_u32_e32 v88, 0, v90
	v_add_u32_e32 v91, s12, v90
	v_mul_f32_e32 v90, 0xbfb8aa3b, v62
	v_exp_f32_e32 v90, v90
	v_mul_f32_e32 v110, 0xbfb8aa3b, v63
	v_exp_f32_e32 v110, v110
	v_pk_fma_f32 v[58:59], v[8:9], v[58:59], 0 op_sel_hi:[1,1,0]
	v_add_f32_e32 v90, 1.0, v90
	v_pk_fma_f32 v[58:59], v[10:11], v[66:67], v[58:59]
	v_pk_mul_f32 v[108:109], v[108:109], v[112:113]
	v_pk_fma_f32 v[58:59], v[12:13], v[78:79], v[58:59]
	v_rcp_f32_e32 v112, v90
	v_pk_fma_f32 v[114:115], v[14:15], v[72:73], v[58:59]
	v_add_f32_e32 v90, 1.0, v110
	v_mul_f32_e32 v58, 0xbfb8aa3b, v114
	v_rcp_f32_e32 v113, v90
	v_exp_f32_e32 v90, v58
	v_mul_f32_e32 v58, 0xbfb8aa3b, v115
	v_exp_f32_e32 v110, v58
	v_pk_mul_f32 v[58:59], v[62:63], v[112:113]
	v_add_f32_e32 v62, 1.0, v90
	v_rcp_f32_e32 v62, v62
	v_add_f32_e32 v63, 1.0, v110
	v_rcp_f32_e32 v63, v63
	v_pk_fma_f32 v[68:69], v[16:17], v[68:69], 0 op_sel_hi:[1,1,0]
	v_pk_mul_f32 v[112:113], v[58:59], v[58:59]
	v_pk_fma_f32 v[68:69], v[18:19], v[74:75], v[68:69]
	v_pk_mul_f32 v[62:63], v[114:115], v[62:63]
	v_pk_fma_f32 v[68:69], v[20:21], v[76:77], v[68:69]
	v_add_f32_e32 v122, v112, v113
	v_pk_fma_f32 v[68:69], v[22:23], v[60:61], v[68:69]
	v_pk_mul_f32 v[112:113], v[62:63], v[62:63]
	v_mul_f32_e32 v110, 0xbfb8aa3b, v68
	v_add_f32_e32 v123, v112, v113
	v_exp_f32_e32 v110, v110
	v_mul_f32_e32 v112, 0xbfb8aa3b, v69
	v_exp_f32_e32 v113, v112
	v_pk_fma_f32 v[66:67], v[8:9], v[66:67], 0 op_sel_hi:[1,1,0]
	v_add_f32_e32 v110, 1.0, v110
	v_pk_fma_f32 v[66:67], v[10:11], v[78:79], v[66:67]
	v_rcp_f32_e32 v112, v110
	v_pk_fma_f32 v[66:67], v[12:13], v[72:73], v[66:67]
	v_add_f32_e32 v110, 1.0, v113
	v_pk_fma_f32 v[114:115], v[14:15], v[54:55], v[66:67]
	v_rcp_f32_e32 v113, v110
	v_mul_f32_e32 v66, 0xbfb8aa3b, v114
	v_exp_f32_e32 v110, v66
	v_mul_f32_e32 v66, 0xbfb8aa3b, v115
	v_exp_f32_e32 v124, v66
	v_pk_mul_f32 v[66:67], v[68:69], v[112:113]
	v_add_f32_e32 v68, 1.0, v110
	v_pk_mul_f32 v[112:113], v[66:67], v[66:67]
	v_add_f32_e32 v69, 1.0, v124
	v_pk_fma_f32 v[84:85], v[0:1], v[84:85], 0 op_sel_hi:[0,1,0]
	v_rcp_f32_e32 v68, v68
	v_rcp_f32_e32 v69, v69
	v_add_f32_e32 v124, v112, v113
	v_pk_mov_b32 v[112:113], v[86:87], v[70:71] op_sel:[1,0]
	v_pk_fma_f32 v[84:85], v[2:3], v[86:87], v[84:85] op_sel_hi:[0,1,1]
	v_pk_fma_f32 v[84:85], v[4:5], v[112:113], v[84:85] op_sel_hi:[0,1,1]
	v_pk_fma_f32 v[84:85], v[6:7], v[70:71], v[84:85] op_sel_hi:[0,1,1]
	v_mul_f32_e32 v86, 0xbfb8aa3b, v84
	v_pk_mul_f32 v[68:69], v[114:115], v[68:69]
	v_exp_f32_e32 v114, v86
	v_mul_f32_e32 v86, 0xbfb8aa3b, v85
	v_exp_f32_e32 v115, v86
	v_pk_mul_f32 v[86:87], v[68:69], v[68:69]
	v_add_f32_e32 v114, 1.0, v114
	v_pk_fma_f32 v[80:81], v[0:1], v[80:81], 0 op_sel:[1,0,0] op_sel_hi:[1,1,0]
	v_add_f32_e32 v115, 1.0, v115
	v_rcp_f32_e32 v114, v114
	v_rcp_f32_e32 v115, v115
	v_add_f32_e32 v125, v86, v87
	v_pk_mov_b32 v[86:87], v[82:83], v[64:65] op_sel:[1,0]
	v_pk_fma_f32 v[80:81], v[2:3], v[82:83], v[80:81] op_sel:[1,0,0]
	v_pk_mul_f32 v[84:85], v[84:85], v[114:115]
	v_pk_fma_f32 v[80:81], v[4:5], v[86:87], v[80:81] op_sel:[1,0,0]
	s_mul_i32 s1, s76, 0x12000
	v_pk_fma_f32 v[80:81], v[6:7], v[64:65], v[80:81] op_sel:[1,0,0]
	s_mul_hi_i32 s0, s76, 0x12000
	v_mul_f32_e32 v82, 0xbfb8aa3b, v80
	v_exp_f32_e32 v114, v82
	v_mul_f32_e32 v82, 0xbfb8aa3b, v81
	v_exp_f32_e32 v115, v82
	s_add_u32 s78, s40, s1
	s_addc_u32 s79, s41, s0
	s_mul_i32 s0, s82, 0x440
	v_readlane_b32 s82, v95, s55
	v_readlane_b32 s83, v95, s33
	v_pk_fma_f32 v[74:75], v[16:17], v[74:75], 0 op_sel_hi:[1,1,0]
	v_pk_fma_f32 v[78:79], v[8:9], v[78:79], 0 op_sel_hi:[1,1,0]
	v_pk_mul_f32 v[82:83], v[84:85], s[82:83]
	v_add_f32_e32 v84, 1.0, v114
	v_rcp_f32_e32 v114, v84
	v_add_f32_e32 v84, 1.0, v115
	v_rcp_f32_e32 v115, v84
	v_pk_fma_f32 v[74:75], v[18:19], v[76:77], v[74:75]
	v_cvt_pk_bf16_f32 v84, v82, v83
	v_pk_fma_f32 v[74:75], v[20:21], v[60:61], v[74:75]
	v_pk_mul_f32 v[80:81], v[80:81], v[114:115]
	v_pk_fma_f32 v[74:75], v[22:23], v[46:47], v[74:75]
	v_pk_mul_f32 v[80:81], v[80:81], s[82:83]
	v_mul_f32_e32 v82, 0xbfb8aa3b, v74
	v_mul_f32_e32 v114, 0xbfb8aa3b, v75
	v_exp_f32_e32 v82, v82
	v_exp_f32_e32 v114, v114
	v_cvt_pk_bf16_f32 v115, v80, v81
	v_pk_fma_f32 v[78:79], v[10:11], v[72:73], v[78:79]
	v_add_f32_e32 v80, 1.0, v82
	v_add_f32_e32 v81, 1.0, v114
	v_rcp_f32_e32 v80, v80
	v_rcp_f32_e32 v81, v81
	v_pk_fma_f32 v[78:79], v[12:13], v[54:55], v[78:79]
	v_and_b32_e32 v118, 32, v215
	v_pk_fma_f32 v[78:79], v[14:15], v[32:33], v[78:79]
	v_pk_mul_f32 v[74:75], v[74:75], v[80:81]
	v_cmp_eq_u32_e32 vcc, 0, v118
	v_pk_mul_f32 v[80:81], v[74:75], v[74:75]
	v_mul_f32_e32 v118, 0xbfb8aa3b, v79
	v_add_f32_e32 v80, v80, v81
	v_mul_f32_e32 v81, 0xbfb8aa3b, v78
	v_exp_f32_e32 v81, v81
	v_exp_f32_e32 v118, v118
	v_add_u32_e32 v89, 0x48, v93
	v_or_b32_e32 v126, 2, v92
	v_add_u32_e32 v83, v126, v89
	v_lshl_add_u32 v114, v83, 1, s12
	v_cndmask_b32_e32 v83, v80, v119, vcc
	v_cndmask_b32_e32 v80, v119, v80, vcc
	ds_bpermute_b32 v119, v105, v80
	v_add_f32_e32 v80, 1.0, v81
	v_add_f32_e32 v81, 1.0, v118
	v_rcp_f32_e32 v80, v80
	v_rcp_f32_e32 v81, v81
	v_pk_fma_f32 v[76:77], v[16:17], v[76:77], 0 op_sel_hi:[1,1,0]
	s_waitcnt lgkmcnt(0)
	v_add_f32_e32 v118, v83, v119
	v_pk_fma_f32 v[76:77], v[18:19], v[60:61], v[76:77]
	v_pk_mul_f32 v[78:79], v[78:79], v[80:81]
	v_pk_fma_f32 v[76:77], v[20:21], v[46:47], v[76:77]
	v_pk_mul_f32 v[80:81], v[78:79], v[78:79]
	v_pk_fma_f32 v[76:77], v[22:23], v[48:49], v[76:77]
	v_add_f32_e32 v80, v80, v81
	v_cndmask_b32_e32 v119, v80, v116, vcc
	v_cndmask_b32_e32 v80, v116, v80, vcc
	v_mul_f32_e32 v81, 0xbfb8aa3b, v76
	v_mul_f32_e32 v116, 0xbfb8aa3b, v77
	v_exp_f32_e32 v81, v81
	v_exp_f32_e32 v116, v116
	v_pk_mul_f32 v[108:109], v[108:109], s[2:3]
	v_add_lshl_u32 v121, v92, v89, 1
	v_cvt_pk_bf16_f32 v108, v108, v109
	v_add_u32_e32 v109, s12, v121
	v_add_u32_e32 v82, 0, v121
	ds_bpermute_b32 v121, v105, v80
	v_add_f32_e32 v80, 1.0, v81
	v_add_f32_e32 v81, 1.0, v116
	v_rcp_f32_e32 v80, v80
	v_rcp_f32_e32 v81, v81
	v_pk_fma_f32 v[72:73], v[8:9], v[72:73], 0 op_sel_hi:[1,1,0]
	s_waitcnt lgkmcnt(0)
	v_add_f32_e32 v116, v119, v121
	v_pk_fma_f32 v[72:73], v[10:11], v[54:55], v[72:73]
	v_pk_mul_f32 v[76:77], v[76:77], v[80:81]
	v_pk_fma_f32 v[72:73], v[12:13], v[32:33], v[72:73]
	v_pk_mul_f32 v[80:81], v[76:77], v[76:77]
	v_pk_fma_f32 v[72:73], v[14:15], v[34:35], v[72:73]
	v_add_f32_e32 v119, v80, v81
	v_mul_f32_e32 v81, 0xbfb8aa3b, v72
	v_mul_f32_e32 v121, 0xbfb8aa3b, v73
	v_exp_f32_e32 v81, v81
	v_exp_f32_e32 v121, v121
	v_cndmask_b32_e32 v80, v117, v119, vcc
	v_add_u32_e32 v127, v126, v93
	ds_bpermute_b32 v126, v105, v80
	v_add_f32_e32 v80, 1.0, v81
	v_add_f32_e32 v81, 1.0, v121
	v_rcp_f32_e32 v80, v80
	v_rcp_f32_e32 v81, v81
	v_pk_fma_f32 v[112:113], v[0:1], v[112:113], 0 op_sel_hi:[0,1,0]
	v_cndmask_b32_e32 v117, v119, v117, vcc
	s_waitcnt lgkmcnt(0)
	v_add_f32_e32 v117, v117, v126
	v_pk_mul_f32 v[80:81], v[72:73], v[80:81]
	v_pk_fma_f32 v[60:61], v[16:17], v[60:61], 0 op_sel_hi:[1,1,0]
	v_pk_mul_f32 v[72:73], v[80:81], v[80:81]
	v_pk_fma_f32 v[60:61], v[18:19], v[46:47], v[60:61]
	v_add_f32_e32 v72, v72, v73
	v_cndmask_b32_e32 v121, v72, v120, vcc
	v_cndmask_b32_e32 v120, v120, v72, vcc
	v_pk_mov_b32 v[72:73], v[70:71], v[28:29] op_sel:[1,0]
	v_pk_fma_f32 v[70:71], v[2:3], v[70:71], v[112:113] op_sel_hi:[0,1,1]
	v_pk_fma_f32 v[70:71], v[4:5], v[72:73], v[70:71] op_sel_hi:[0,1,1]
	v_pk_fma_f32 v[70:71], v[6:7], v[28:29], v[70:71] op_sel_hi:[0,1,1]
	v_mul_f32_e32 v112, 0xbfb8aa3b, v71
	v_exp_f32_e32 v112, v112
	v_mul_f32_e32 v113, 0xbfb8aa3b, v70
	v_exp_f32_e32 v126, v113
	v_pk_fma_f32 v[60:61], v[20:21], v[48:49], v[60:61]
	v_add_f32_e32 v112, 1.0, v112
	v_rcp_f32_e32 v113, v112
	v_add_f32_e32 v112, 1.0, v126
	v_rcp_f32_e32 v112, v112
	v_readlane_b32 s92, v95, s4
	v_readlane_b32 s93, v95, s5
	v_pk_fma_f32 v[86:87], v[0:1], v[86:87], 0 op_sel:[1,0,0] op_sel_hi:[1,1,0]
	v_pk_mul_f32 v[70:71], v[70:71], v[112:113]
	v_pk_fma_f32 v[60:61], v[22:23], v[50:51], v[60:61]
	v_pk_mul_f32 v[112:113], v[70:71], s[92:93]
	v_pk_mov_b32 v[70:71], v[64:65], v[24:25] op_sel:[1,0]
	v_pk_fma_f32 v[64:65], v[2:3], v[64:65], v[86:87] op_sel:[1,0,0]
	v_mul_f32_e32 v86, 0xbfb8aa3b, v60
	v_mul_f32_e32 v87, 0xbfb8aa3b, v61
	v_exp_f32_e32 v86, v86
	v_exp_f32_e32 v87, v87
	v_pk_fma_f32 v[54:55], v[8:9], v[54:55], 0 op_sel_hi:[1,1,0]
	v_pk_fma_f32 v[16:17], v[16:17], v[46:47], 0 op_sel_hi:[1,1,0]
	v_add_f32_e32 v86, 1.0, v86
	v_add_f32_e32 v87, 1.0, v87
	v_rcp_f32_e32 v86, v86
	v_rcp_f32_e32 v87, v87
	v_pk_fma_f32 v[8:9], v[8:9], v[32:33], 0 op_sel_hi:[1,1,0]
	v_pk_fma_f32 v[54:55], v[10:11], v[32:33], v[54:55]
	v_pk_fma_f32 v[16:17], v[18:19], v[48:49], v[16:17]
	v_pk_mul_f32 v[60:61], v[60:61], v[86:87]
	v_pk_fma_f32 v[8:9], v[10:11], v[34:35], v[8:9]
	v_pk_mul_f32 v[86:87], v[60:61], v[60:61]
	v_pk_fma_f32 v[54:55], v[12:13], v[34:35], v[54:55]
	v_add_f32_e32 v86, v86, v87
	v_pk_fma_f32 v[16:17], v[20:21], v[50:51], v[16:17]
	v_pk_fma_f32 v[8:9], v[12:13], v[36:37], v[8:9]
	v_cndmask_b32_e32 v87, v122, v86, vcc
	v_pk_fma_f32 v[54:55], v[14:15], v[36:37], v[54:55]
	v_pk_fma_f32 v[16:17], v[22:23], v[52:53], v[16:17]
	v_pk_fma_f32 v[8:9], v[14:15], v[40:41], v[8:9]
	v_lshlrev_b32_e32 v30, 16, v96
	v_and_b32_e32 v26, 0xffff0000, v96
	v_lshl_add_u32 v96, s0, 1, v97
	s_mul_i32 s0, s54, 0x88
	ds_bpermute_b32 v128, v105, v87
	v_cvt_pk_bf16_f32 v129, v112, v113
	v_mul_f32_e32 v112, 0xbfb8aa3b, v54
	v_mul_f32_e32 v113, 0xbfb8aa3b, v55
	v_mul_f32_e32 v18, 0xbfb8aa3b, v16
	v_mul_f32_e32 v19, 0xbfb8aa3b, v17
	v_mul_f32_e32 v10, 0xbfb8aa3b, v8
	v_mul_f32_e32 v11, 0xbfb8aa3b, v9
	v_lshl_add_u32 v106, s0, 1, v97
	v_readlane_b32 s0, v253, 45
	v_exp_f32_e32 v112, v112
	v_exp_f32_e32 v113, v113
	v_exp_f32_e32 v18, v18
	v_exp_f32_e32 v19, v19
	v_exp_f32_e32 v10, v10
	v_exp_f32_e32 v11, v11
	v_lshl_add_u32 v90, s0, 1, v97
	v_readlane_b32 s0, v253, 46
	v_and_b32_e32 v111, 16, v215
	v_cndmask_b32_e32 v86, v86, v122, vcc
	v_lshl_add_u32 v110, s0, 1, v97
	v_readlane_b32 s0, v253, 47
	s_waitcnt lgkmcnt(0)
	v_add_f32_e32 v86, v86, v128
	v_add_f32_e32 v112, 1.0, v112
	v_lshl_add_u32 v83, s0, 1, v97
	v_readlane_b32 s0, v253, 48
	v_add_f32_e32 v113, 1.0, v113
	v_add_f32_e32 v18, 1.0, v18
	v_lshl_add_u32 v119, s0, 1, v97
	v_cmp_eq_u32_e64 s[0:1], 0, v111
	v_add_f32_e32 v19, 1.0, v19
	v_add_f32_e32 v10, 1.0, v10
	v_add_f32_e32 v11, 1.0, v11
	v_cndmask_b32_e64 v111, v86, v118, s[0:1]
	v_cndmask_b32_e64 v86, v118, v86, s[0:1]
	v_rcp_f32_e32 v112, v112
	v_rcp_f32_e32 v113, v113
	v_rcp_f32_e32 v18, v18
	v_rcp_f32_e32 v19, v19
	v_rcp_f32_e32 v10, v10
	v_rcp_f32_e32 v11, v11
	ds_bpermute_b32 v86, v103, v86
	v_pk_mul_f32 v[54:55], v[54:55], v[112:113]
	v_pk_mul_f32 v[16:17], v[16:17], v[18:19]
	v_pk_mul_f32 v[8:9], v[8:9], v[10:11]
	v_pk_mul_f32 v[112:113], v[54:55], v[54:55]
	v_pk_mul_f32 v[18:19], v[16:17], v[16:17]
	v_pk_mul_f32 v[10:11], v[8:9], v[8:9]
	s_waitcnt lgkmcnt(0)
	v_add_f32_e32 v86, v111, v86
	v_add_f32_e32 v111, v112, v113
	v_add_f32_e32 v18, v18, v19
	v_add_f32_e32 v10, v10, v11
	v_cndmask_b32_e32 v112, v111, v123, vcc
	v_cndmask_b32_e32 v111, v123, v111, vcc
	v_cndmask_b32_e32 v19, v18, v124, vcc
	v_cndmask_b32_e32 v18, v124, v18, vcc
	v_cndmask_b32_e32 v11, v125, v10, vcc
	ds_bpermute_b32 v120, v105, v120
	ds_bpermute_b32 v111, v105, v111
	ds_bpermute_b32 v12, v105, v18
	ds_bpermute_b32 v11, v105, v11
	v_cndmask_b32_e32 v10, v10, v125, vcc
	s_waitcnt lgkmcnt(3)
	v_add_f32_e32 v120, v121, v120
	s_waitcnt lgkmcnt(2)
	v_add_f32_e32 v20, v112, v111
	s_waitcnt lgkmcnt(1)
	v_add_f32_e32 v12, v19, v12
	s_waitcnt lgkmcnt(0)
	v_add_f32_e32 v10, v10, v11
	v_cndmask_b32_e64 v21, v20, v116, s[0:1]
	v_cndmask_b32_e64 v20, v116, v20, s[0:1]
	v_cndmask_b32_e64 v13, v117, v12, s[0:1]
	v_cndmask_b32_e64 v11, v120, v10, s[0:1]
	ds_bpermute_b32 v20, v103, v20
	ds_bpermute_b32 v13, v103, v13
	ds_bpermute_b32 v11, v103, v11
	v_and_b32_e32 v104, 8, v215
	v_cndmask_b32_e64 v12, v12, v117, s[0:1]
	v_cndmask_b32_e64 v10, v10, v120, s[0:1]
	s_waitcnt lgkmcnt(2)
	v_add_f32_e32 v14, v21, v20
	s_waitcnt lgkmcnt(1)
	v_add_f32_e32 v12, v12, v13
	v_cmp_eq_u32_e32 vcc, 0, v104
	s_waitcnt lgkmcnt(0)
	v_add_f32_e32 v10, v10, v11
	v_lshlrev_b32_e32 v31, 16, v99
	v_cndmask_b32_e32 v13, v12, v86, vcc
	v_cndmask_b32_e32 v12, v86, v12, vcc
	v_cndmask_b32_e32 v11, v14, v10, vcc
	ds_bpermute_b32 v12, v102, v12
	ds_bpermute_b32 v11, v102, v11
	v_and_b32_e32 v27, 0xffff0000, v99
	v_and_b32_e32 v99, 4, v215
	v_pk_fma_f32 v[64:65], v[4:5], v[70:71], v[64:65] op_sel:[1,0,0]
	v_cndmask_b32_e32 v10, v10, v14, vcc
	v_pk_fma_f32 v[64:65], v[6:7], v[24:25], v[64:65] op_sel:[1,0,0]
	s_waitcnt lgkmcnt(1)
	v_add_f32_e32 v12, v13, v12
	s_waitcnt lgkmcnt(0)
	v_add_f32_e32 v10, v10, v11
	v_cmp_eq_u32_e32 vcc, 0, v99
	v_lshl_add_u32 v85, v127, 1, s12
	v_mul_f32_e32 v127, 0xbfb8aa3b, v65
	v_mul_f32_e32 v118, 0xbfb8aa3b, v64
	v_cndmask_b32_e32 v13, v12, v10, vcc
	v_cndmask_b32_e32 v10, v10, v12, vcc
	v_exp_f32_e32 v127, v127
	v_exp_f32_e32 v118, v118
	ds_bpermute_b32 v12, v101, v10
	v_readlane_b32 s0, v253, 49
	v_add_f32_e32 v87, 1.0, v127
	v_add_f32_e32 v15, 1.0, v118
	v_rcp_f32_e32 v87, v87
	v_rcp_f32_e32 v86, v15
	s_waitcnt lgkmcnt(0)
	v_add_f32_e32 v12, v13, v12
	ds_bpermute_b32 v13, v100, v12
	v_lshl_add_u32 v33, s0, 1, v97
	v_pk_mul_f32 v[10:11], v[64:65], v[86:87]
	v_readlane_b32 s0, v253, 50
	v_pk_mul_f32 v[10:11], v[10:11], s[92:93]
	s_mov_b32 s74, 0x358637bd
	v_cvt_pk_bf16_f32 v23, v10, v11
	s_waitcnt lgkmcnt(0)
	v_add_f32_e32 v10, v12, v13
	ds_bpermute_b32 v11, v98, v10
	v_or_b32_e32 v121, 4, v92
	v_lshl_add_u32 v34, s0, 1, v97
	v_add_u32_e32 v14, v121, v89
	v_lshl_add_u32 v32, v14, 1, s12
	s_waitcnt lgkmcnt(0)
	v_add_f32_e32 v35, v10, v11
	v_mov_b64_e32 v[10:11], s[74:75]
	v_readlane_b32 s1, v35, 0
	v_readlane_b32 s0, v35, 4
	v_readlane_b32 s80, v94, s95
	v_readlane_b32 s81, v94, s54
	v_pk_add_f32 v[12:13], s[0:1], v[10:11] op_sel_hi:[1,0]
	v_readlane_b32 s20, v94, s55
	v_readlane_b32 s21, v94, s33
	v_rsq_f32_e32 v13, v13
	v_rsq_f32_e32 v14, v12
	v_mov_b32_e32 v12, v13
	v_mul_f32_e32 v12, 0x3db504f3, v12
	v_pk_mul_f32 v[12:13], v[44:45], v[12:13] op_sel_hi:[1,0]
	v_readlane_b32 s1, v35, 8
	v_cvt_pk_bf16_f32 v12, v12, v13
	v_readlane_b32 s0, v35, 12
	ds_write_b32 v96, v12 offset:34816
	v_pk_mul_f32 v[14:15], v[38:39], v[14:15] op_sel_hi:[1,0]
	v_pk_add_f32 v[12:13], s[0:1], v[10:11] op_sel_hi:[1,0]
	v_cvt_pk_bf16_f32 v36, v14, v15
	v_readlane_b32 s22, v94, s4
	v_rsq_f32_e32 v13, v13
	v_rsq_f32_e32 v18, v12
	v_mov_b32_e32 v12, v13
	v_mul_f32_e32 v12, 0x3db504f3, v12
	v_pk_mul_f32 v[12:13], v[56:57], v[12:13] op_sel_hi:[1,0]
	v_pk_mul_f32 v[18:19], v[42:43], v[18:19] op_sel_hi:[1,0]
	v_cvt_pk_bf16_f32 v12, v12, v13
	v_cvt_pk_bf16_f32 v37, v18, v19
	ds_write_b32 v106, v12 offset:34816
	v_mov_b32_e32 v12, v14
	v_mov_b32_e32 v13, v18
	v_mov_b32_e32 v18, v15
	v_pk_mul_f32 v[12:13], s[2:3], v[12:13]
	v_pk_mul_f32 v[14:15], s[2:3], v[18:19]
	v_pk_mul_f32 v[20:21], s[80:81], v[12:13]
	v_cvt_pk_bf16_f32 v12, v12, v14
	v_pk_mul_f32 v[18:19], s[80:81], v[14:15]
	ds_write2st64_b32 v96, v36, v12 offset1:68
	v_cvt_pk_bf16_f32 v12, v13, v15
	v_cvt_pk_bf16_f32 v20, v20, v21
	ds_write2st64_b32 v106, v37, v12 offset1:68
	ds_write_b32 v88, v107 offset:52224
	ds_write_b32 v91, v20
	ds_write_b32 v88, v108 offset:52368
	v_cvt_pk_bf16_f32 v12, v18, v19
	v_readlane_b32 s1, v35, 16
	v_readlane_b32 s0, v35, 20
	ds_write_b32 v109, v12
	v_readlane_b32 s23, v94, s5
	v_pk_add_f32 v[12:13], s[0:1], v[10:11] op_sel_hi:[1,0]
	v_add_u32_e32 v126, v121, v93
	v_lshl_add_u32 v22, v126, 1, s12
	v_rsq_f32_e32 v13, v13
	v_rsq_f32_e32 v14, v12
	v_mov_b32_e32 v12, v13
	v_mul_f32_e32 v12, 0x3db504f3, v12
	v_pk_mul_f32 v[12:13], v[62:63], v[12:13] op_sel_hi:[1,0]
	v_readlane_b32 s1, v35, 24
	v_cvt_pk_bf16_f32 v12, v12, v13
	v_readlane_b32 s0, v35, 28
	ds_write_b32 v90, v12 offset:34816
	v_pk_mul_f32 v[14:15], v[58:59], v[14:15] op_sel_hi:[1,0]
	v_pk_add_f32 v[12:13], s[0:1], v[10:11] op_sel_hi:[1,0]
	v_cvt_pk_bf16_f32 v36, v14, v15
	v_readlane_b32 s96, v95, s6
	v_rsq_f32_e32 v13, v13
	v_rsq_f32_e32 v18, v12
	v_mov_b32_e32 v12, v13
	v_mul_f32_e32 v12, 0x3db504f3, v12
	v_pk_mul_f32 v[12:13], v[68:69], v[12:13] op_sel_hi:[1,0]
	v_pk_mul_f32 v[18:19], v[66:67], v[18:19] op_sel_hi:[1,0]
	v_cvt_pk_bf16_f32 v12, v12, v13
	v_cvt_pk_bf16_f32 v37, v18, v19
	ds_write_b32 v110, v12 offset:34816
	v_mov_b32_e32 v12, v14
	v_mov_b32_e32 v13, v18
	v_mov_b32_e32 v18, v15
	v_pk_mul_f32 v[12:13], s[82:83], v[12:13]
	v_pk_mul_f32 v[14:15], s[82:83], v[18:19]
	v_pk_mul_f32 v[20:21], s[20:21], v[12:13]
	v_cvt_pk_bf16_f32 v12, v12, v14
	v_pk_mul_f32 v[18:19], s[20:21], v[14:15]
	ds_write2st64_b32 v90, v36, v12 offset1:68
	v_cvt_pk_bf16_f32 v12, v13, v15
	v_cvt_pk_bf16_f32 v20, v20, v21
	ds_write2st64_b32 v110, v37, v12 offset1:68
	ds_write_b32 v88, v84 offset:52228
	ds_write_b32 v85, v20
	ds_write_b32 v82, v115 offset:52228
	v_cvt_pk_bf16_f32 v12, v18, v19
	v_readlane_b32 s1, v35, 32
	v_readlane_b32 s0, v35, 36
	ds_write_b32 v114, v12
	v_readlane_b32 s97, v95, s7
	v_pk_add_f32 v[12:13], s[0:1], v[10:11] op_sel_hi:[1,0]
	v_readlane_b32 s34, v94, s6
	v_readlane_b32 s35, v94, s7
	v_rsq_f32_e32 v13, v13
	v_rsq_f32_e32 v14, v12
	v_mov_b32_e32 v12, v13
	v_mul_f32_e32 v12, 0x3db504f3, v12
	v_pk_mul_f32 v[12:13], v[78:79], v[12:13] op_sel_hi:[1,0]
	v_pk_mul_f32 v[14:15], v[74:75], v[14:15] op_sel_hi:[1,0]
	v_cvt_pk_bf16_f32 v12, v12, v13
	v_readlane_b32 s1, v35, 40
	v_readlane_b32 s0, v35, 44
	v_cvt_pk_bf16_f32 v18, v14, v15
	ds_write_b32 v83, v12 offset:34816
	v_pk_add_f32 v[12:13], s[0:1], v[10:11] op_sel_hi:[1,0]
	ds_write_b32 v83, v18
	s_mov_b64 s[2:3], -1
	v_rsq_f32_e32 v13, v13
	v_rsq_f32_e32 v18, v12
	v_mov_b32_e32 v12, v13
	v_mul_f32_e32 v12, 0x3db504f3, v12
	v_pk_mul_f32 v[12:13], v[80:81], v[12:13] op_sel_hi:[1,0]
	v_pk_mul_f32 v[18:19], v[76:77], v[18:19] op_sel_hi:[1,0]
	v_cvt_pk_bf16_f32 v12, v12, v13
	v_cvt_pk_bf16_f32 v20, v18, v19
	ds_write_b32 v119, v12 offset:34816
	v_mov_b32_e32 v12, v14
	v_mov_b32_e32 v13, v18
	v_mov_b32_e32 v18, v15
	v_pk_mul_f32 v[12:13], s[92:93], v[12:13]
	v_pk_mul_f32 v[14:15], s[92:93], v[18:19]
	ds_write_b32 v119, v20
	v_pk_mul_f32 v[20:21], s[22:23], v[12:13]
	v_cvt_pk_bf16_f32 v12, v12, v14
	v_pk_mul_f32 v[18:19], s[22:23], v[14:15]
	ds_write_b32 v83, v12 offset:17408
	v_cvt_pk_bf16_f32 v12, v13, v15
	v_cvt_pk_bf16_f32 v20, v20, v21
	ds_write_b32 v119, v12 offset:17408
	ds_write_b32 v88, v129 offset:52232
	ds_write_b32 v22, v20
	ds_write_b32 v82, v23 offset:52232
	v_cvt_pk_bf16_f32 v12, v18, v19
	v_readlane_b32 s1, v35, 48
	v_readlane_b32 s0, v35, 52
	ds_write_b32 v32, v12
	s_nop 0
	v_pk_add_f32 v[12:13], s[0:1], v[10:11] op_sel_hi:[1,0]
	s_nop 0
	s_nop 0
	v_rsq_f32_e32 v13, v13
	v_rsq_f32_e32 v14, v12
	v_mov_b32_e32 v12, v13
	v_mul_f32_e32 v12, 0x3db504f3, v12
	v_pk_mul_f32 v[12:13], v[54:55], v[12:13] op_sel_hi:[1,0]
	v_readlane_b32 s1, v35, 56
	v_readlane_b32 s0, v35, 60
	v_cvt_pk_bf16_f32 v12, v12, v13
	ds_write_b32 v33, v12 offset:34816
	v_pk_add_f32 v[10:11], s[0:1], v[10:11] op_sel_hi:[1,0]
	v_pk_mul_f32 v[14:15], v[60:61], v[14:15] op_sel_hi:[1,0]
	v_cvt_pk_bf16_f32 v18, v14, v15
	v_rsq_f32_e32 v11, v11
	v_rsq_f32_e32 v12, v10
	ds_write_b32 v33, v18
	v_mov_b32_e32 v10, v11
	v_mul_f32_e32 v10, 0x3db504f3, v10
	v_pk_mul_f32 v[8:9], v[8:9], v[10:11] op_sel_hi:[1,0]
	v_pk_mul_f32 v[10:11], v[16:17], v[12:13] op_sel_hi:[1,0]
	v_pk_fma_f32 v[16:17], v[0:1], v[72:73], 0 op_sel_hi:[0,1,0]
	v_cvt_pk_bf16_f32 v12, v10, v11
	ds_write_b32 v34, v12
	v_pk_mov_b32 v[12:13], v[28:29], v[30:31] op_sel:[1,0]
	v_pk_fma_f32 v[16:17], v[2:3], v[28:29], v[16:17] op_sel_hi:[0,1,1]
	v_pk_fma_f32 v[12:13], v[4:5], v[12:13], v[16:17] op_sel_hi:[0,1,1]
	v_pk_fma_f32 v[12:13], v[6:7], v[30:31], v[12:13] op_sel_hi:[0,1,1]
	v_mul_f32_e32 v16, 0xbfb8aa3b, v13
	v_exp_f32_e32 v16, v16
	v_mul_f32_e32 v17, 0xbfb8aa3b, v12
	v_exp_f32_e32 v17, v17
	v_cvt_pk_bf16_f32 v18, v8, v9
	v_add_f32_e32 v8, 1.0, v16
	v_rcp_f32_e32 v9, v8
	v_add_f32_e32 v8, 1.0, v17
	v_rcp_f32_e32 v8, v8
	v_pk_fma_f32 v[0:1], v[0:1], v[70:71], 0 op_sel:[1,0,0] op_sel_hi:[1,1,0]
	ds_write_b32 v34, v18 offset:34816
	v_pk_fma_f32 v[0:1], v[2:3], v[24:25], v[0:1] op_sel:[1,0,0]
	v_pk_mul_f32 v[8:9], v[12:13], v[8:9]
	v_pk_mov_b32 v[12:13], v[24:25], v[26:27] op_sel:[1,0]
	v_pk_mul_f32 v[8:9], v[8:9], s[96:97]
	v_pk_fma_f32 v[0:1], v[4:5], v[12:13], v[0:1] op_sel:[1,0,0]
	v_cvt_pk_bf16_f32 v18, v8, v9
	v_pk_fma_f32 v[0:1], v[6:7], v[26:27], v[0:1] op_sel:[1,0,0]
	v_mov_b32_e32 v8, v14
	v_mul_f32_e32 v2, 0xbfb8aa3b, v1
	v_exp_f32_e32 v4, v2
	v_mul_f32_e32 v2, 0xbfb8aa3b, v0
	v_exp_f32_e32 v6, v2
	v_mov_b32_e32 v9, v10
	v_add_f32_e32 v4, 1.0, v4
	v_rcp_f32_e32 v5, v4
	v_add_f32_e32 v4, 1.0, v6
	v_rcp_f32_e32 v4, v4
	v_pk_mul_f32 v[8:9], s[96:97], v[8:9]
	v_mov_b32_e32 v10, v15
	v_pk_mul_f32 v[2:3], s[34:35], v[8:9]
	v_pk_mul_f32 v[0:1], v[0:1], v[4:5]
	v_or_b32_e32 v16, 6, v92
	v_pk_mul_f32 v[0:1], v[0:1], s[96:97]
	v_cvt_pk_bf16_f32 v6, v2, v3
	v_cvt_pk_bf16_f32 v4, v0, v1
	v_pk_mul_f32 v[0:1], s[96:97], v[10:11]
	v_add_u32_e32 v17, v16, v93
	v_pk_mul_f32 v[2:3], s[34:35], v[0:1]
	v_cvt_pk_bf16_f32 v0, v8, v0
	v_add_u32_e32 v12, v16, v89
	ds_write_b32 v33, v0 offset:17408
	v_cvt_pk_bf16_f32 v0, v9, v1
	v_lshl_add_u32 v7, v17, 1, s12
	ds_write_b32 v34, v0 offset:17408
	ds_write_b32 v88, v18 offset:52236
	ds_write_b32 v7, v6
	ds_write_b32 v82, v4 offset:52236
	v_cvt_pk_bf16_f32 v0, v2, v3
	v_lshl_add_u32 v1, v12, 1, s12
	ds_write_b32 v1, v0
	s_waitcnt lgkmcnt(0)
	s_barrier
	s_cmp_lg_u32 s95, 0
	s_cbranch_scc1 .Lgpf_done_next
	v_readlane_b32 s99, v253, 10
	s_nop 0
	s_add_i32 s99, s76, s99
	s_cmpk_lt_i32 s99, 0x800
	s_cbranch_scc0 .Lgpf_done_next
	v_readlane_b32 s100, v253, 17
	s_lshr_b32 s0, s99, 8
	s_lshl_b32 s0, s0, 12
	s_and_b32 s1, s99, 63
	s_lshl_b32 s101, s1, 6
	s_add_i32 s0, s0, s101
	s_or_b32 s1, s1, s100
	s_bfe_u32 s101, s99, 0x20006
	v_add_u32_e32 v219, s0, v237
	v_lshlrev_b32_e32 v219, 5, v219
	s_lshl_b32 s99, s101, 2
	v_add_u32_e32 v219, s99, v219
	s_lshl_b32 s100, s100, 3
	s_add_i32 s0, s0, s100
	s_lshl_b32 s0, s0, 10
	s_lshl_b32 s101, s101, 8
	s_add_i32 s0, s0, s101
	v_lshlrev_b32_e32 v217, 2, v237
	v_add_u32_e32 v217, s0, v217
	v_add_u32_e32 v218, 0x1000, v217
	s_add_u32 s100, s88, 0x200000
	s_addc_u32 s101, s89, 0
	s_cmp_eq_u32 s1, 0
	s_cbranch_scc1 .Lgpf_zero_next
	global_load_dword v172, v217, s[44:45] offset:-3072 nt
	global_load_dword v173, v217, s[68:69] offset:-3072 nt
	global_load_dword v174, v217, s[72:73] offset:-3072 nt
	global_load_dword v175, v217, s[44:45] offset:-2048 nt
	global_load_dword v176, v217, s[68:69] offset:-2048 nt
	global_load_dword v177, v217, s[72:73] offset:-2048 nt
	global_load_dword v178, v217, s[44:45] offset:-1024 nt
	global_load_dword v179, v217, s[68:69] offset:-1024 nt
	global_load_dword v180, v217, s[72:73] offset:-1024 nt
	s_branch .Lgpf_rest_next

.LBB0_329:
	v_readlane_b32 s20, v253, 43
	v_readlane_b32 s21, v253, 44
	s_mov_b64 s[0:1], -1
	s_and_b64 vcc, exec, s[20:21]
	s_waitcnt lgkmcnt(0)
	s_barrier
	s_cbranch_vccz .LBB0_338
	v_readlane_b32 s99, v253, 10
	s_nop 0
	s_add_i32 s99, s76, s99
	s_cmpk_lt_i32 s99, 0x800
	s_cbranch_scc0 .Lgpf_done_nxd
	v_readlane_b32 s100, v253, 17
	s_lshr_b32 s0, s99, 8
	s_lshl_b32 s0, s0, 12
	s_and_b32 s1, s99, 63
	s_lshl_b32 s101, s1, 6
	s_add_i32 s0, s0, s101
	s_or_b32 s1, s1, s100
	s_bfe_u32 s101, s99, 0x20006
	v_add_u32_e32 v219, s0, v237
	v_lshlrev_b32_e32 v219, 5, v219
	s_lshl_b32 s99, s101, 2
	v_add_u32_e32 v219, s99, v219
	s_lshl_b32 s100, s100, 3
	s_add_i32 s0, s0, s100
	s_lshl_b32 s0, s0, 10
	s_lshl_b32 s101, s101, 8
	s_add_i32 s0, s0, s101
	v_lshlrev_b32_e32 v217, 2, v237
	v_add_u32_e32 v217, s0, v217
	v_add_u32_e32 v218, 0x1000, v217
	s_add_u32 s100, s88, 0x200000
	s_addc_u32 s101, s89, 0
	s_cmp_eq_u32 s1, 0
	s_cbranch_scc1 .Lgpf_zero_nxd
	global_load_dword v172, v217, s[44:45] offset:-3072 nt
	global_load_dword v173, v217, s[68:69] offset:-3072 nt
	global_load_dword v174, v217, s[72:73] offset:-3072 nt
	global_load_dword v175, v217, s[44:45] offset:-2048 nt
	global_load_dword v176, v217, s[68:69] offset:-2048 nt
	global_load_dword v177, v217, s[72:73] offset:-2048 nt
	global_load_dword v178, v217, s[44:45] offset:-1024 nt
	global_load_dword v179, v217, s[68:69] offset:-1024 nt
	global_load_dword v180, v217, s[72:73] offset:-1024 nt
	s_branch .Lgpf_rest_nxd

.Lgpf_done_nxd:
	s_mov_b64 s[0:1], -1
	v_and_b32_e32 v0, 31, v215
	v_lshrrev_b32_e32 v1, 5, v215
	v_mul_u32_u24_e32 v2, 0x110, v0
	v_lshl_add_u32 v2, v1, 3, v2
	v_add_u32_e32 v2, 0x8800, v2
	v_lshlrev_b32_e32 v3, 2, v0
	v_add_u32_e32 v3, 0x1c600, v3
	v_mul_u32_u24_e32 v4, 0x440, v1
	v_lshl_add_u32 v4, v0, 1, v4
	v_lshlrev_b32_e32 v5, 4, v1
	v_add_u32_e32 v5, 0x1c700, v5
	v_lshlrev_b32_e32 v6, 4, v215
	s_add_i32 s34, s82, -1
	s_cmp_gt_u32 s34, 31
	s_cbranch_scc1 .Lgp_rd_done
	s_cmp_gt_u32 s34, 15
	s_cbranch_scc1 .Lgp_rk0
	s_lshr_b32 s20, s34, 3
	s_mul_i32 s21, s20, 0x2200
	s_lshl_b32 s22, s34, 5
	s_and_b32 s22, s22, 0xe0
	s_add_i32 s21, s21, s22
	v_add_u32_e32 v8, s21, v2
	ds_read2_b64 v[16:19], v8 offset1:2
	s_lshl_b32 s20, s20, 7
	v_add_u32_e32 v9, s20, v3
	ds_read_b32 v20, v9
	s_branch .Lgp_rn0
